# scan helper waves: per-channel parameter vectors loaded once per unit into registers (their per-chunk loads forced two vmcnt(0) drains of the operand prefetch each chunk); prefetch drain moved behind
# speedup vs baseline: 1.0333x; 1.0026x over previous
; __device__ __forceinline__ u32x4 pk8(const f32x4 a, const f32x4 b) { u32x4 w; w.x = cvt_pk_bf16(a[0], a[1]); w.y = cvt_pk_bf16(a[2], a[3]); w.z = cvt_pk_bf16(b[0], b[1]); w.w = cvt_pk_bf16(b[2], b[3]); return w; }
; #define LAS __attribute__((address_space(3)))
; __device__ __forceinline__ void scan_unit(Frame& F, const Args& a, int layer, int unit) {
;     ...
;         const int ht = tid - 256, tl = ht >> 3, c8 = ht & 7, ch = hh * 64 + c8 * 8;
;         const int pr = ht >> 4, c4 = ht & 15, chp = hh * 64 + c4 * 4;
;         const size_t po = (size_t)layer * 1024 + ch, pop = (size_t)layer * 1024 + chp;
;         struct HelpIn { v2u r0, k0, v0, e0, a0, r1, k1, v1, e1, a1, k2, v2, e2, a2, k3; v4u gt; };
;         HelpIn cur, nxt;
;     ...
;         unsigned long long ph_act = 0ull;
;     ...
;         HELP_LOAD(cur, 0, -2);
;     ...
;                 for (int i = 0; i < 2; ++i) o_[i] = (y_[i] * rstd * *(const f32x4*)(a.in[14] + po + 4 * i) + *(const f32x4*)(a.in[15] + po + 4 * i) + bon * v_[i]) * g_[i];
;                 *(v4u*)(YA + row * 1024 + ch) = pk8(o_[0], o_[1]);
;             }
;             if (it < NCH) {
;                 LAS float* buf = bufs + (it & 1) * SC_BUF;
;                 const f32x4 pkk_ = *(const f32x4*)(a.in[11] + pop), pka_ = *(const f32x4*)(a.in[12] + pop), prk_ = *(const f32x4*)(a.in[13] + pop);
.LBB0_1318:
	v_readlane_b32 s2, v253, 41
	v_readlane_b32 s3, v253, 42
	v_mbcnt_lo_u32_b32 v1, -1, 0
	v_mbcnt_hi_u32_b32 v1, -1, v1
	s_mov_b64 s[0:1], -1
	v_add_u32_e32 v125, s27, v1
	s_and_b64 vcc, exec, s[2:3]
	v_and_b32_e32 v124, 15, v1
	s_cbranch_vccz .LBB0_1336
	s_add_u32 s36, s18, 0x1a400000
	s_addc_u32 s37, s19, 0
	s_add_u32 s6, s18, 0x3c400000
	s_addc_u32 s7, s19, 0
	s_add_u32 s20, s18, 0x38400000
	s_addc_u32 s21, s19, 0
	v_add_u32_e32 v20, 0xffffff00, v125
	v_and_b32_e32 v126, 7, v1
	s_lshl_b32 s1, s22, 6
	s_ashr_i32 s0, s22, 4
	s_and_b32 s1, s1, 0x3c0
	v_lshlrev_b32_e32 v21, 3, v126
	v_ashrrev_i32_e32 v22, 4, v20
	v_lshlrev_b32_e32 v127, 2, v124
	v_or_b32_e32 v7, s1, v21
	v_or_b32_e32 v16, s1, v127
	v_lshlrev_b32_e32 v2, 1, v22
	s_ashr_i32 s1, s0, 31
	s_lshl_b64 s[2:3], s[0:1], 12
	v_ashrrev_i32_e32 v3, 31, v2
	v_lshl_add_u64 v[10:11], s[2:3], 0, v[2:3]
	v_mov_b64_e32 v[12:13], s[36:37]
	s_movk_i32 s23, 0x1800
	v_mad_u64_u32 v[14:15], s[36:37], v10, s23, v[12:13]
	v_or_b32_e32 v4, s60, v16
	v_mad_i32_i24 v15, v11, s23, v15
	v_lshlrev_b32_e32 v16, 1, v16
	v_mov_b32_e32 v17, v0
	v_lshl_add_u64 v[14:15], v[14:15], 0, v[16:17]
	global_load_dwordx2 v[82:83], v[14:15], off
	global_load_dwordx2 v[100:101], v[14:15], off offset:2048
	v_add_co_u32_e32 v14, vcc, s9, v14
	v_lshlrev_b64 v[10:11], 11, v[10:11]
	s_nop 0
	v_addc_co_u32_e32 v15, vcc, 0, v15, vcc
	global_load_dwordx2 v[80:81], v[14:15], off
	v_lshl_add_u64 v[14:15], s[20:21], 0, v[10:11]
	v_lshl_add_u64 v[10:11], s[6:7], 0, v[10:11]
	v_lshl_add_u64 v[14:15], v[14:15], 0, v[16:17]
	v_lshl_add_u64 v[10:11], v[10:11], 0, v[16:17]
	global_load_dwordx2 v[78:79], v[14:15], off
	global_load_dwordx2 v[84:85], v[10:11], off
	v_or_b32_e32 v10, 1, v2
	v_ashrrev_i32_e32 v11, 31, v10
	v_lshl_add_u64 v[14:15], s[2:3], 0, v[10:11]
	v_mad_u64_u32 v[18:19], s[36:37], v14, s23, v[12:13]
	v_mad_i32_i24 v19, v15, s23, v19
	v_lshl_add_u64 v[18:19], v[18:19], 0, v[16:17]
	global_load_dwordx2 v[88:89], v[18:19], off
	global_load_dwordx2 v[102:103], v[18:19], off offset:2048
	v_add_co_u32_e32 v18, vcc, s9, v18
	v_lshlrev_b64 v[14:15], 11, v[14:15]
	s_nop 0
	v_addc_co_u32_e32 v19, vcc, 0, v19, vcc
	global_load_dwordx2 v[92:93], v[18:19], off
	v_lshl_add_u64 v[18:19], s[20:21], 0, v[14:15]
	v_lshl_add_u64 v[14:15], s[6:7], 0, v[14:15]
	v_lshl_add_u64 v[18:19], v[18:19], 0, v[16:17]
	v_lshl_add_u64 v[14:15], v[14:15], 0, v[16:17]
	global_load_dwordx2 v[86:87], v[18:19], off
	global_load_dwordx2 v[90:91], v[14:15], off
	v_add_u32_e32 v14, 2, v2
	v_ashrrev_i32_e32 v15, 31, v14
	v_lshl_add_u64 v[14:15], s[2:3], 0, v[14:15]
	v_mad_u64_u32 v[18:19], s[36:37], v14, s23, v[12:13]
	v_mad_i32_i24 v19, v15, s23, v19
	v_lshl_add_u64 v[18:19], v[18:19], 0, v[16:17]
	global_load_dwordx2 v[104:105], v[18:19], off offset:2048
	v_add_co_u32_e32 v18, vcc, s9, v18
	v_lshlrev_b64 v[14:15], 11, v[14:15]
	s_nop 0
	v_addc_co_u32_e32 v19, vcc, 0, v19, vcc
	global_load_dwordx2 v[98:99], v[18:19], off
	v_lshl_add_u64 v[18:19], s[20:21], 0, v[14:15]
	v_lshl_add_u64 v[14:15], s[6:7], 0, v[14:15]
	v_lshl_add_u64 v[14:15], v[14:15], 0, v[16:17]
	global_load_dwordx2 v[96:97], v[14:15], off
	v_add_u32_e32 v14, 3, v2
	v_ashrrev_i32_e32 v15, 31, v14
	v_lshl_add_u64 v[14:15], s[2:3], 0, v[14:15]
	v_mad_u64_u32 v[12:13], s[6:7], v14, s23, v[12:13]
	v_mad_i32_i24 v13, v15, s23, v13
	v_lshl_add_u64 v[18:19], v[18:19], 0, v[16:17]
	v_lshl_add_u64 v[12:13], v[12:13], 0, v[16:17]
	global_load_dwordx2 v[94:95], v[18:19], off
	global_load_dwordx2 v[106:107], v[12:13], off offset:2048
	v_ashrrev_i32_e32 v6, 3, v20
	v_or_b32_e32 v8, s60, v7
	v_lshlrev_b32_e32 v12, 1, v7
	v_ashrrev_i32_e32 v7, 31, v6
	v_lshl_add_u64 v[14:15], s[2:3], 0, v[6:7]
	v_lshl_or_b32 v128, v6, 6, v21
	v_and_b32_e32 v6, 3, v1
	v_mov_b32_e32 v13, v0
	s_add_i32 s2, 0, 0x17200
	v_lshlrev_b32_e32 v135, 7, v6
	v_lshlrev_b32_e32 v137, 4, v6
	v_lshlrev_b32_e32 v6, 1, v1
	v_lshl_add_u64 v[12:13], s[18:19], 0, v[12:13]
	v_lshl_add_u32 v129, v128, 2, s2
	v_and_b32_e32 v138, 8, v6
	s_movk_i32 s2, 0x50
	v_lshlrev_b64 v[6:7], 11, v[14:15]
	v_mul_lo_u32 v139, v22, s2
	v_lshl_add_u64 v[6:7], v[12:13], 0, v[6:7]
	s_mov_b64 s[2:3], 0x40400000
	v_lshl_add_u64 v[30:31], v[6:7], 0, s[2:3]
	s_lshl_b32 s2, s5, 1
	v_lshlrev_b32_e32 v17, 3, v124
	s_and_b32 s2, s2, 0x780
	v_or_b32_e32 v42, s2, v17
	s_mul_i32 s2, s0, 0x1800000
	v_mov_b32_e32 v5, v0
	v_readlane_b32 s44, v251, 18
	s_mul_hi_i32 s3, s0, 0x1800000
	s_add_u32 s2, s18, s2
	v_readlane_b32 s50, v251, 24
	v_readlane_b32 s51, v251, 25
	v_readlane_b32 s52, v251, 26
	v_readlane_b32 s53, v251, 27
	v_readlane_b32 s54, v251, 28
	v_readlane_b32 s55, v251, 29
	v_lshlrev_b64 v[4:5], 2, v[4:5]
	s_addc_u32 s3, s19, s3
	s_lshl_b64 s[0:1], s[0:1], 23
	v_mov_b32_e32 v9, v0
	v_lshl_add_u64 v[36:37], s[50:51], 0, v[4:5]
	v_lshl_add_u64 v[38:39], s[52:53], 0, v[4:5]
	v_lshl_add_u64 v[40:41], s[54:55], 0, v[4:5]
	v_mov_b64_e32 v[4:5], s[2:3]
	s_add_u32 s0, s18, s0
	v_and_b32_e32 v11, -8, v20
	v_bfe_u32 v16, v1, 2, 2
	v_and_b32_e32 v18, -16, v20
	v_bfe_u32 v19, v1, 1, 3
	v_lshlrev_b64 v[6:7], 2, v[8:9]
	v_readlane_b32 s56, v251, 30
	v_readlane_b32 s57, v251, 31
	v_readlane_b32 s58, v251, 32
	v_readlane_b32 s59, v251, 33
	v_mad_i64_i32 v[44:45], s[2:3], v2, s23, v[4:5]
	v_lshlrev_b64 v[2:3], 11, v[2:3]
	s_addc_u32 s1, s19, s1
	v_lshlrev_b32_e32 v130, 8, v22
	v_lshlrev_b32_e32 v131, 9, v22
	v_lshlrev_b32_e32 v132, 8, v10
	v_lshlrev_b32_e32 v133, 10, v22
	v_lshlrev_b32_e32 v134, 6, v124
	v_and_b32_e32 v136, 64, v17
	v_cmp_eq_u32_e64 s[40:41], 0, v124
	v_lshlrev_b32_e32 v140, 5, v10
	v_lshl_add_u64 v[32:33], s[56:57], 0, v[6:7]
	v_lshl_add_u64 v[34:35], s[58:59], 0, v[6:7]
	v_mov_b32_e32 v43, v0
	v_lshl_add_u64 v[46:47], s[0:1], 0, v[2:3]
	s_mov_b32 s0, -2
	v_lshlrev_b32_e32 v141, 2, v11
	v_lshlrev_b32_e32 v142, 3, v16
	v_lshlrev_b32_e32 v143, 2, v18
	v_lshlrev_b32_e32 v144, 2, v19
	v_readlane_b32 s45, v251, 19
	v_readlane_b32 s46, v251, 20
	v_readlane_b32 s47, v251, 21
	v_readlane_b32 s48, v251, 22
	v_readlane_b32 s49, v251, 23
	global_load_dwordx4 v[176:179], v[32:33], off
	global_load_dwordx4 v[180:183], v[32:33], off offset:16
	global_load_dwordx4 v[184:187], v[34:35], off
	global_load_dwordx4 v[188:191], v[34:35], off offset:16
	global_load_dwordx4 v[192:195], v[36:37], off
	global_load_dwordx4 v[196:199], v[38:39], off
	global_load_dwordx4 v[200:203], v[40:41], off
	s_waitcnt vmcnt(0)
	s_branch .LBB0_1322

; __device__ __forceinline__ void scan_unit(Frame& F, const Args& a, int layer, int unit) {
;     ...
;             cur = nxt;
;     ...
;             asm volatile("s_waitcnt vmcnt(0) lgkmcnt(0)" ::: "memory"); ph_act += __builtin_amdgcn_s_memtime() - ph0;
;     ...
;             __syncthreads();
.LBB0_1321:
	s_mov_b64 s[2:3], 0x30000
	s_add_i32 s0, s0, 1
	v_lshl_add_u64 v[44:45], v[44:45], 0, s[2:3]
	s_mov_b64 s[2:3], 0x10000
	v_lshl_add_u64 v[46:47], v[46:47], 0, s[2:3]
	s_cmpk_lg_i32 s0, 0x80
	s_waitcnt lgkmcnt(0)
	s_barrier
	s_waitcnt vmcnt(0)
	v_mov_b64_e32 v[20:21], v[4:5]
	v_mov_b64_e32 v[18:19], v[2:3]
	v_mov_b64_e32 v[106:107], v[76:77]
	v_mov_b64_e32 v[96:97], v[74:75]
	v_mov_b64_e32 v[94:95], v[72:73]
	v_mov_b64_e32 v[98:99], v[66:67]
	v_mov_b64_e32 v[104:105], v[64:65]
	v_mov_b64_e32 v[90:91], v[60:61]
	v_mov_b64_e32 v[86:87], v[62:63]
	v_mov_b64_e32 v[92:93], v[68:69]
	v_mov_b64_e32 v[102:103], v[70:71]
	v_mov_b64_e32 v[88:89], v[54:55]
	v_mov_b64_e32 v[84:85], v[56:57]
	v_mov_b64_e32 v[78:79], v[58:59]
	v_mov_b64_e32 v[80:81], v[48:49]
	v_mov_b64_e32 v[100:101], v[50:51]
	v_mov_b64_e32 v[82:83], v[52:53]
	s_cbranch_scc0 .LBB0_1335

; __device__ __forceinline__ void scan_unit(Frame& F, const Args& a, int layer, int unit) {
;     ...
;                 const LAS float* buf = bufs + (it & 1) * SC_BUF; const LAS float* yb = sY + (it & 1) * SC_VEC;
;                 const size_t row = (size_t)b * SEQ + (size_t)(it - 2) * SC + tl; const int o = tl * 64 + c8 * 8;
;                 f32x4 y_[2], v_[2], g_[2];
; #pragma unroll
;                 for (int i = 0; i < 2; ++i) { y_[i] = *(const LAS f32x4*)(yb + o + 4 * i); v_[i] = *(const LAS f32x4*)(buf + SC_VP + o + 4 * i); }
;                 const float bon = buf[SC_BON + tl * 8 + c8];
;                 unpk8(cur.gt, g_[0], g_[1]);
;                 const float s1 = ((y_[0].x + y_[0].y) + (y_[0].z + y_[0].w)) + ((y_[1].x + y_[1].y) + (y_[1].z + y_[1].w));
;                 const float mu = sum8(s1) * (1.f / 64.f);
;                 float s2 = 0.f;
; #pragma unroll
;                 for (int i = 0; i < 2; ++i) { y_[i] = y_[i] - mu; const f32x4 q = y_[i] * y_[i]; s2 += (q.x + q.y) + (q.z + q.w); }
;                 const float rstd = __builtin_amdgcn_rsqf(sum8(s2) * (1.f / 64.f) + 64e-5f);
;                 f32x4 o_[2];
; #pragma unroll
;                 for (int i = 0; i < 2; ++i) o_[i] = (y_[i] * rstd * *(const f32x4*)(a.in[14] + po + 4 * i) + *(const f32x4*)(a.in[15] + po + 4 * i) + bon * v_[i]) * g_[i];
;                 *(v4u*)(YA + row * 1024 + ch) = pk8(o_[0], o_[1]);
;     ...
;                 const f32x4 pkk_ = *(const f32x4*)(a.in[11] + pop), pka_ = *(const f32x4*)(a.in[12] + pop), prk_ = *(const f32x4*)(a.in[13] + pop);
;                 const f32x4 zk0 = UNP4(cur.k0), zk1 = UNP4(cur.k1), zk2 = UNP4(cur.k2), zk3 = UNP4(cur.k3);
;                 f32x4 kn0 = zk0 * pkk_, kn1 = zk1 * pkk_, kn2 = zk2 * pkk_, kn3 = zk3 * pkk_;
;                 kn0 = kn0 * __builtin_amdgcn_rsqf(fmaxf(SUM16(DOT4(kn0, kn0)), 1e-24f)); kn1 = kn1 * __builtin_amdgcn_rsqf(fmaxf(SUM16(DOT4(kn1, kn1)), 1e-24f));
;                 kn2 = kn2 * __builtin_amdgcn_rsqf(fmaxf(SUM16(DOT4(kn2, kn2)), 1e-24f)); kn3 = kn3 * __builtin_amdgcn_rsqf(fmaxf(SUM16(DOT4(kn3, kn3)), 1e-24f));
;                 const f32x4 r0 = UNP4(cur.r0), r1 = UNP4(cur.r1), v0 = UNP4(cur.v0), v1 = UNP4(cur.v1), v2 = UNP4(cur.v2);
;                 const f32x4 ar0 = UNP4(cur.a0), ar1 = UNP4(cur.a1), ar2 = UNP4(cur.a2);
;                 const f32x4 e0 = UNP4(cur.e0), e1 = UNP4(cur.e1), e2 = UNP4(cur.e2);
.LBB0_1332:
	s_and_b32 s1, s20, 1
	s_mul_i32 s2, s1, 0xb900
	s_add_i32 s2, s2, 0
	v_lshl_add_u32 v10, s1, 13, v129
	v_lshl_add_u32 v6, v128, 2, s2
	ds_read_b128 v[14:17], v6 offset:38144
	ds_read_b128 v[6:9], v6 offset:38160
	ds_read_b128 v[22:25], v10
	ds_read_b128 v[10:13], v10 offset:16
	v_lshlrev_b32_e32 v26, 2, v126
	v_add3_u32 v26, s2, v141, v26
	v_lshlrev_b32_e32 v114, 16, v18
	v_and_b32_e32 v115, 0xffff0000, v18
	v_lshlrev_b32_e32 v116, 16, v19
	v_and_b32_e32 v117, 0xffff0000, v19
	v_lshlrev_b32_e32 v110, 16, v20
	v_and_b32_e32 v111, 0xffff0000, v20
	v_lshlrev_b32_e32 v112, 16, v21
	v_and_b32_e32 v113, 0xffff0000, v21
	s_waitcnt lgkmcnt(0)
	v_mov_b32_e32 v18, v22
	v_mov_b32_e32 v19, v10
	v_mov_b32_e32 v20, v23
	v_mov_b32_e32 v21, v11
	ds_read_b32 v108, v26 offset:46336
	v_pk_add_f32 v[18:19], v[18:19], v[20:21]
	v_mov_b32_e32 v20, v24
	v_mov_b32_e32 v21, v12
	v_mov_b32_e32 v26, v25
	v_mov_b32_e32 v27, v13
	v_pk_add_f32 v[20:21], v[20:21], v[26:27]
	s_mov_b32 s1, s31
	v_pk_add_f32 v[18:19], v[18:19], v[20:21]
	s_lshl_b64 s[2:3], s[0:1], 16
	v_add_f32_e32 v18, v18, v19
	s_nop 1
	v_add_f32_dpp v18, v18, v18 quad_perm:[1,0,3,2] row_mask:0xf bank_mask:0xf bound_ctrl:1
	s_nop 1
	v_add_f32_dpp v18, v18, v18 quad_perm:[2,3,0,1] row_mask:0xf bank_mask:0xf bound_ctrl:1
	s_nop 1
	v_add_f32_dpp v26, v18, v18 row_half_mirror row_mask:0xf bank_mask:0xf bound_ctrl:1
	v_fmamk_f32 v19, v26, 0xbc800000, v23
	v_fmamk_f32 v18, v26, 0xbc800000, v22
	v_fmamk_f32 v119, v26, 0xbc800000, v11
	v_fmamk_f32 v118, v26, 0xbc800000, v10
	v_fmamk_f32 v25, v26, 0xbc800000, v25
	v_fmac_f32_e32 v24, 0xbc800000, v26
	v_pk_mul_f32 v[22:23], v[18:19], v[18:19]
	v_fmamk_f32 v13, v26, 0xbc800000, v13
	v_fmac_f32_e32 v12, 0xbc800000, v26
	v_pk_mul_f32 v[26:27], v[118:119], v[118:119]
	v_pk_mul_f32 v[20:21], v[24:25], v[24:25]
	v_pk_mul_f32 v[10:11], v[12:13], v[12:13]
	v_mov_b32_e32 v28, v22
	v_mov_b32_e32 v29, v26
	v_mov_b32_e32 v26, v23
	v_pk_add_f32 v[22:23], v[28:29], v[26:27]
	v_mov_b32_e32 v26, v20
	v_mov_b32_e32 v27, v10
	v_mov_b32_e32 v10, v21
	v_pk_add_f32 v[10:11], v[26:27], v[10:11]
	s_nop 0
	v_pk_add_f32 v[10:11], v[22:23], v[10:11]
	s_nop 0
	v_add_f32_e32 v10, v10, v11
	s_nop 1
	v_add_f32_dpp v10, v10, v10 quad_perm:[1,0,3,2] row_mask:0xf bank_mask:0xf bound_ctrl:1
	s_nop 1
	v_add_f32_dpp v10, v10, v10 quad_perm:[2,3,0,1] row_mask:0xf bank_mask:0xf bound_ctrl:1
	s_nop 1
	v_add_f32_dpp v10, v10, v10 row_half_mirror row_mask:0xf bank_mask:0xf bound_ctrl:1
	v_fmamk_f32 v10, v10, 0x3c800000, v243
	v_rsq_f32_e32 v120, v10
	s_nop 0
	v_pk_mul_f32 v[10:11], v[18:19], v[120:121] op_sel_hi:[1,0]
	v_pk_mul_f32 v[122:123], v[24:25], v[120:121] op_sel_hi:[1,0]
	v_pk_mul_f32 v[12:13], v[12:13], v[120:121] op_sel_hi:[1,0]
	v_pk_fma_f32 v[28:29], v[178:179], v[122:123], v[186:187]
	v_pk_fma_f32 v[10:11], v[176:177], v[10:11], v[184:185]
	v_pk_fma_f32 v[12:13], v[182:183], v[12:13], v[190:191]
	s_waitcnt lgkmcnt(0)
	v_pk_fma_f32 v[14:15], v[14:15], v[108:109], v[10:11] op_sel_hi:[1,0,1]
	v_pk_fma_f32 v[10:11], v[16:17], v[108:109], v[28:29] op_sel_hi:[1,0,1]
	v_pk_mul_f32 v[16:17], v[118:119], v[120:121] op_sel_hi:[1,0]
	v_pk_mul_f32 v[14:15], v[14:15], v[114:115]
	v_pk_fma_f32 v[16:17], v[180:181], v[16:17], v[188:189]
	v_pk_mul_f32 v[10:11], v[10:11], v[116:117]
	v_pk_fma_f32 v[16:17], v[6:7], v[108:109], v[16:17] op_sel_hi:[1,0,1]
	v_pk_fma_f32 v[6:7], v[8:9], v[108:109], v[12:13] op_sel_hi:[1,0,1]
	v_pk_mul_f32 v[8:9], v[16:17], v[110:111]
	v_pk_mul_f32 v[6:7], v[6:7], v[112:113]
	v_cvt_pk_bf16_f32 v12, v14, v15
	v_cvt_pk_bf16_f32 v13, v10, v11
	v_cvt_pk_bf16_f32 v14, v8, v9
	s_nop 0
	v_cvt_pk_bf16_f32 v15, v6, v7
	v_lshl_add_u64 v[6:7], v[30:31], 0, s[2:3]
	global_store_dwordx4 v[6:7], v[12:15], off
	s_cmpk_gt_u32 s20, 0x7f
	s_cbranch_scc1 .LBB0_1321
.LBB0_1333:
	s_nop 1
	v_mov_b64_e32 v[14:15], v[192:193]
	v_mov_b64_e32 v[16:17], v[194:195]
	v_mov_b64_e32 v[10:11], v[196:197]
	v_mov_b64_e32 v[12:13], v[198:199]
	v_mov_b64_e32 v[6:7], v[200:201]
	v_mov_b64_e32 v[8:9], v[202:203]
	v_lshlrev_b32_e32 v118, 16, v100
	v_and_b32_e32 v119, 0xffff0000, v100
	v_lshlrev_b32_e32 v120, 16, v101
	v_and_b32_e32 v121, 0xffff0000, v101
	v_lshlrev_b32_e32 v108, 16, v102
	v_and_b32_e32 v109, 0xffff0000, v102
	v_lshlrev_b32_e32 v116, 16, v103
	v_and_b32_e32 v117, 0xffff0000, v103
	v_lshlrev_b32_e32 v112, 16, v104
	v_and_b32_e32 v113, 0xffff0000, v104
	v_lshlrev_b32_e32 v114, 16, v105
	v_and_b32_e32 v115, 0xffff0000, v105
	v_lshlrev_b32_e32 v18, 16, v106
	v_and_b32_e32 v19, 0xffff0000, v106
	v_lshlrev_b32_e32 v20, 16, v107
	v_and_b32_e32 v21, 0xffff0000, v107
	v_and_b32_e32 v156, 0xffff0000, v98
	v_lshlrev_b32_e32 v158, 16, v99
	v_and_b32_e32 v160, 0xffff0000, v99
	v_lshlrev_b32_e32 v99, 16, v87
	v_and_b32_e32 v87, 0xffff0000, v87
	v_and_b32_e32 v149, 0xffff0000, v81
	s_bitcmp1_b32 s20, 0
	v_and_b32_e32 v151, 0xffff0000, v92
	v_lshlrev_b32_e32 v152, 16, v93
	v_and_b32_e32 v153, 0xffff0000, v93
	v_lshlrev_b32_e32 v150, 16, v92
	v_lshlrev_b32_e32 v92, 16, v90
	v_and_b32_e32 v93, 0xffff0000, v90
	v_lshlrev_b32_e32 v90, 16, v91
	v_and_b32_e32 v91, 0xffff0000, v91
	v_lshlrev_b32_e32 v154, 16, v96
	v_and_b32_e32 v155, 0xffff0000, v96
	v_lshlrev_b32_e32 v96, 16, v97
	v_and_b32_e32 v97, 0xffff0000, v97
	s_cselect_b32 s1, 0xb900, 0
	s_add_i32 s1, s1, 0
	v_mov_b32_e32 v157, v0
	v_mov_b32_e32 v159, v0
	v_mov_b32_e32 v161, v0
	v_pk_mul_f32 v[22:23], v[14:15], v[118:119]
	v_pk_mul_f32 v[24:25], v[16:17], v[120:121]
	v_pk_mul_f32 v[26:27], v[14:15], v[108:109]
	v_pk_mul_f32 v[28:29], v[16:17], v[116:117]
	v_pk_mul_f32 v[100:101], v[14:15], v[112:113]
	v_pk_mul_f32 v[102:103], v[16:17], v[114:115]
; #define UNP4(W) ((f32x4){bflo((W).x), bfhi((W).x), bflo((W).y), bfhi((W).y)})
; #define EXP4(E) ((f32x4){__builtin_amdgcn_exp2f(-1.44269504f * (E).x), __builtin_amdgcn_exp2f(-1.44269504f * (E).y), __builtin_amdgcn_exp2f(-1.44269504f * (E).z), __builtin_amdgcn_exp2f(-1.44269504f * (E).w)})
; #define SUM16(X) sum16_ns(X)
; __device__ __forceinline__ void scan_unit(Frame& F, const Args& a, int layer, int unit) {
;     ...
;                 const f32x4 zk0 = UNP4(cur.k0), zk1 = UNP4(cur.k1), zk2 = UNP4(cur.k2), zk3 = UNP4(cur.k3);
;                 f32x4 kn0 = zk0 * pkk_, kn1 = zk1 * pkk_, kn2 = zk2 * pkk_, kn3 = zk3 * pkk_;
;                 kn0 = kn0 * __builtin_amdgcn_rsqf(fmaxf(SUM16(DOT4(kn0, kn0)), 1e-24f)); kn1 = kn1 * __builtin_amdgcn_rsqf(fmaxf(SUM16(DOT4(kn1, kn1)), 1e-24f));
;                 kn2 = kn2 * __builtin_amdgcn_rsqf(fmaxf(SUM16(DOT4(kn2, kn2)), 1e-24f)); kn3 = kn3 * __builtin_amdgcn_rsqf(fmaxf(SUM16(DOT4(kn3, kn3)), 1e-24f));
;                 const f32x4 r0 = UNP4(cur.r0), r1 = UNP4(cur.r1), v0 = UNP4(cur.v0), v1 = UNP4(cur.v1), v2 = UNP4(cur.v2);
;                 const f32x4 ar0 = UNP4(cur.a0), ar1 = UNP4(cur.a1), ar2 = UNP4(cur.a2);
;                 const f32x4 e0 = UNP4(cur.e0), e1 = UNP4(cur.e1), e2 = UNP4(cur.e2);
;                 const f32x4 w0 = EXP4(e0), w1 = EXP4(e1), w2 = EXP4(e2);
;                 const f32x4 a1v = -kn1, a2v = -kn2, a3v = -kn3;
;                 const f32x4 b0 = kn0 * ar0, b1 = kn1 * ar1, b2 = kn2 * ar2;
;                 const f32x4 kp0 = zk0 * (1.f + (ar0 - 1.f) * pka_), kp1 = zk1 * (1.f + (ar1 - 1.f) * pka_), kp2 = zk2 * (1.f + (ar2 - 1.f) * pka_);
;                 const f32x4 W2 = w0 * w1, Bt = b0 * w1, Kt = kp0 * w1, x0v = a2v, x1v = w2 * a3v;
	v_pk_mul_f32 v[20:21], v[16:17], v[20:21]
	v_pk_mul_f32 v[18:19], v[14:15], v[18:19]
	v_pk_mul_f32 v[14:15], v[24:25], v[24:25]
	v_pk_mul_f32 v[16:17], v[22:23], v[22:23]
	v_pk_mul_f32 v[104:105], v[28:29], v[28:29]
	v_pk_mul_f32 v[106:107], v[26:27], v[26:27]
	v_pk_mov_b32 v[146:147], v[16:17], v[14:15] op_sel:[1,0]
	v_mov_b32_e32 v17, v15
	v_pk_mov_b32 v[14:15], v[106:107], v[104:105] op_sel:[1,0]
	v_mov_b32_e32 v107, v105
	v_pk_mul_f32 v[110:111], v[102:103], v[102:103]
	v_pk_mul_f32 v[122:123], v[100:101], v[100:101]
	v_pk_add_f32 v[16:17], v[146:147], v[16:17]
	v_pk_add_f32 v[14:15], v[14:15], v[106:107]
	v_pk_mov_b32 v[104:105], v[122:123], v[110:111] op_sel:[1,0]
	v_mov_b32_e32 v123, v111
	v_add_f32_e32 v16, v16, v17
	v_add_f32_e32 v14, v14, v15
	v_mul_f32_e32 v145, v19, v19
	v_mul_f32_e32 v148, v21, v21
	v_pk_add_f32 v[104:105], v[104:105], v[122:123]
	v_add_f32_dpp v16, v16, v16 quad_perm:[1,0,3,2] row_mask:0xf bank_mask:0xf bound_ctrl:1
	v_add_f32_dpp v14, v14, v14 quad_perm:[1,0,3,2] row_mask:0xf bank_mask:0xf bound_ctrl:1
	v_fmac_f32_e32 v145, v18, v18
	v_fmac_f32_e32 v148, v20, v20
	v_add_f32_e32 v15, v104, v105
	v_add_f32_e32 v106, v145, v148
	v_lshlrev_b32_e32 v122, 16, v98
	v_add_f32_dpp v15, v15, v15 quad_perm:[1,0,3,2] row_mask:0xf bank_mask:0xf bound_ctrl:1
	v_add_f32_dpp v16, v16, v16 quad_perm:[2,3,0,1] row_mask:0xf bank_mask:0xf bound_ctrl:1
	v_add_f32_dpp v14, v14, v14 quad_perm:[2,3,0,1] row_mask:0xf bank_mask:0xf bound_ctrl:1
	v_add_f32_dpp v17, v106, v106 quad_perm:[1,0,3,2] row_mask:0xf bank_mask:0xf bound_ctrl:1
	v_lshlrev_b32_e32 v98, 16, v86
	v_and_b32_e32 v86, 0xffff0000, v86
	v_add_f32_dpp v15, v15, v15 quad_perm:[2,3,0,1] row_mask:0xf bank_mask:0xf bound_ctrl:1
	v_add_f32_dpp v16, v16, v16 row_half_mirror row_mask:0xf bank_mask:0xf bound_ctrl:1
	v_add_f32_dpp v14, v14, v14 row_half_mirror row_mask:0xf bank_mask:0xf bound_ctrl:1
	v_add_f32_dpp v17, v17, v17 quad_perm:[2,3,0,1] row_mask:0xf bank_mask:0xf bound_ctrl:1
	v_lshlrev_b32_e32 v110, 16, v95
	v_and_b32_e32 v95, 0xffff0000, v95
	v_add_f32_dpp v15, v15, v15 row_half_mirror row_mask:0xf bank_mask:0xf bound_ctrl:1
	v_add_f32_dpp v16, v16, v16 row_mirror row_mask:0xf bank_mask:0xf bound_ctrl:1
	v_add_f32_dpp v14, v14, v14 row_mirror row_mask:0xf bank_mask:0xf bound_ctrl:1
	v_add_f32_dpp v17, v17, v17 row_half_mirror row_mask:0xf bank_mask:0xf bound_ctrl:1
	v_lshlrev_b32_e32 v146, 16, v80
	v_max_f32_e32 v16, v16, v16
	v_add_f32_dpp v15, v15, v15 row_mirror row_mask:0xf bank_mask:0xf bound_ctrl:1
	v_max_f32_e32 v14, v14, v14
	v_add_f32_dpp v107, v17, v17 row_mirror row_mask:0xf bank_mask:0xf bound_ctrl:1
	v_max_f32_e32 v16, 0x179abe15, v16
	v_max_f32_e32 v17, 0x179abe15, v14
	v_max_f32_e32 v15, v15, v15
	v_rsq_f32_e32 v14, v16
	v_rsq_f32_e32 v16, v17
	v_max_f32_e32 v15, 0x179abe15, v15
	v_rsq_f32_e32 v106, v15
	v_pk_mul_f32 v[104:105], v[26:27], v[16:17] op_sel_hi:[1,0]
	v_pk_mul_f32 v[26:27], v[28:29], v[16:17] op_sel_hi:[1,0]
	v_max_f32_e32 v28, v107, v107
	v_max_f32_e32 v28, 0x179abe15, v28
	v_pk_mul_f32 v[24:25], v[24:25], v[14:15] op_sel_hi:[1,0]
	v_pk_mul_f32 v[22:23], v[22:23], v[14:15] op_sel_hi:[1,0]
	v_pk_mul_f32 v[16:17], v[100:101], v[106:107] op_sel_hi:[1,0]
	v_pk_mul_f32 v[14:15], v[102:103], v[106:107] op_sel_hi:[1,0]
	v_rsq_f32_e32 v106, v28
	v_lshlrev_b32_e32 v28, 16, v88
	v_and_b32_e32 v29, 0xffff0000, v88
	v_lshlrev_b32_e32 v88, 16, v78
	v_and_b32_e32 v78, 0xffff0000, v78
	v_lshlrev_b32_e32 v100, 16, v82
	v_and_b32_e32 v101, 0xffff0000, v82
	v_lshlrev_b32_e32 v102, 16, v83
	v_and_b32_e32 v103, 0xffff0000, v83
	v_lshlrev_b32_e32 v82, 16, v89
	v_and_b32_e32 v83, 0xffff0000, v89
	v_lshlrev_b32_e32 v89, 16, v79
	v_mul_f32_e32 v78, 0xbfb8aa3b, v78
	v_and_b32_e32 v79, 0xffff0000, v79
	v_exp_f32_e32 v163, v78
	v_mul_f32_e32 v78, 0xbfb8aa3b, v89
	v_exp_f32_e32 v164, v78
	v_mul_f32_e32 v78, 0xbfb8aa3b, v79
	v_exp_f32_e32 v165, v78
	v_mul_f32_e32 v78, 0xbfb8aa3b, v98
	v_exp_f32_e32 v166, v78
	v_mul_f32_e32 v78, 0xbfb8aa3b, v86
	v_exp_f32_e32 v167, v78
	v_mul_f32_e32 v78, 0xbfb8aa3b, v99
	v_lshlrev_b32_e32 v107, 16, v94
	v_exp_f32_e32 v168, v78
	v_mul_f32_e32 v78, 0xbfb8aa3b, v87
	v_and_b32_e32 v94, 0xffff0000, v94
	v_exp_f32_e32 v169, v78
	v_mul_f32_e32 v78, 0xbfb8aa3b, v107
	v_exp_f32_e32 v170, v78
	v_mul_f32_e32 v78, 0xbfb8aa3b, v94
	v_exp_f32_e32 v171, v78
	v_mul_f32_e32 v78, 0xbfb8aa3b, v110
	v_and_b32_e32 v147, 0xffff0000, v80
	v_lshlrev_b32_e32 v148, 16, v81
	v_lshlrev_b32_e32 v80, 16, v84
	v_and_b32_e32 v81, 0xffff0000, v84
	v_mul_f32_e32 v88, 0xbfb8aa3b, v88
	v_exp_f32_e32 v172, v78
	v_mul_f32_e32 v78, 0xbfb8aa3b, v95
	v_lshlrev_b32_e32 v84, 16, v85
	v_and_b32_e32 v85, 0xffff0000, v85
	v_exp_f32_e32 v162, v88
	v_exp_f32_e32 v173, v78
	v_pk_add_f32 v[78:79], v[80:81], -1.0 op_sel_hi:[1,0]
	v_pk_mul_f32 v[98:99], v[20:21], v[106:107] op_sel_hi:[1,0] neg_lo:[0,1] neg_hi:[0,1]
	v_pk_mul_f32 v[20:21], v[22:23], v[80:81]
	v_pk_add_f32 v[80:81], v[84:85], -1.0 op_sel_hi:[1,0]
	v_pk_fma_f32 v[78:79], v[78:79], v[10:11], 1.0 op_sel_hi:[1,1,0]
	v_pk_mul_f32 v[22:23], v[24:25], v[84:85]
	v_pk_mul_f32 v[24:25], v[26:27], v[90:91]
	v_pk_mul_f32 v[88:89], v[104:105], v[92:93]
	v_pk_fma_f32 v[84:85], v[80:81], v[12:13], 1.0 op_sel_hi:[1,1,0]
	v_pk_mul_f32 v[80:81], v[78:79], v[118:119]
	v_pk_add_f32 v[78:79], v[90:91], -1.0 op_sel_hi:[1,0]
	v_pk_add_f32 v[86:87], v[92:93], -1.0 op_sel_hi:[1,0]
	v_pk_add_f32 v[90:91], v[96:97], -1.0 op_sel_hi:[1,0]
	v_pk_add_f32 v[92:93], v[154:155], -1.0 op_sel_hi:[1,0]
	v_pk_mul_f32 v[84:85], v[84:85], v[120:121]
	v_pk_fma_f32 v[86:87], v[86:87], v[10:11], 1.0 op_sel_hi:[1,1,0]
	v_pk_fma_f32 v[78:79], v[78:79], v[12:13], 1.0 op_sel_hi:[1,1,0]
; #define LAS __attribute__((address_space(3)))
; __device__ __forceinline__ void scan_unit(Frame& F, const Args& a, int layer, int unit) {
;     ...
;                 const f32x4 W2 = w0 * w1, Bt = b0 * w1, Kt = kp0 * w1, x0v = a2v, x1v = w2 * a3v;
;                 const f32x4 X0 = W2 * x0v, X1 = W2 * x1v, X2 = w0 * r0, X3 = W2 * r1;
;                 *(LAS f32x4*)(buf + SC_WW + pr * 64 + c4 * 4) = W2;
;                 *(LAS f32x4*)(buf + SC_VP + (2 * pr) * 64 + c4 * 4) = v0; *(LAS f32x4*)(buf + SC_VP + (2 * pr + 1) * 64 + c4 * 4) = v1;
;                 { LAS f32x4* vq = (LAS f32x4*)(buf + SC_VQ + pr * 256 + c4 * 16);
;                   vq[0] = (f32x4){v0.x, v1.x, v2.x, 0.f}; vq[1] = (f32x4){v0.y, v1.y, v2.y, 0.f}; vq[2] = (f32x4){v0.z, v1.z, v2.z, 0.f}; vq[3] = (f32x4){v0.w, v1.w, v2.w, 0.f}; }
;                 { LAS v2u* bkp = (LAS v2u*)(buf + SC_BK + pr * 128) + (((c4 & 3) * 4) * 4 + (c4 >> 2));
;                   bkp[0] = (v2u){cvt_pk_bf16(Bt.x, Kt.x), cvt_pk_bf16(b1.x, kp1.x)}; bkp[4] = (v2u){cvt_pk_bf16(Bt.y, Kt.y), cvt_pk_bf16(b1.y, kp1.y)};
;                   bkp[8] = (v2u){cvt_pk_bf16(Bt.z, Kt.z), cvt_pk_bf16(b1.z, kp1.z)}; bkp[12] = (v2u){cvt_pk_bf16(Bt.w, Kt.w), cvt_pk_bf16(b1.w, kp1.w)}; }
;                 { LAS unsigned char* xp = (LAS unsigned char*)(buf + SC_XA) + pr * 512 + (c4 >> 3) * 64 + (c4 & 3) * 16 + ((c4 >> 2) & 1) * 8;
;                   *(LAS v2u*)xp = (v2u){cvt_pk_bf16(X0.x, X0.y), cvt_pk_bf16(X0.z, X0.w)}; *(LAS v2u*)(xp + 128) = (v2u){cvt_pk_bf16(X1.x, X1.y), cvt_pk_bf16(X1.z, X1.w)};
;                   *(LAS v2u*)(xp + 256) = (v2u){cvt_pk_bf16(X2.x, X2.y), cvt_pk_bf16(X2.z, X2.w)}; *(LAS v2u*)(xp + 384) = (v2u){cvt_pk_bf16(X3.x, X3.y), cvt_pk_bf16(X3.z, X3.w)}; }
;                 const f32x4 ca = (f32x4){SUM16(DOT4(Bt, x0v)), SUM16(DOT4(Kt, x0v)), SUM16(DOT4(b1, x0v)), SUM16(DOT4(kp1, x0v))};
;                 const f32x4 cb = (f32x4){SUM16(DOT4(Bt, x1v)), SUM16(DOT4(Kt, x1v)), SUM16(DOT4(b1, x1v)), SUM16(DOT4(kp1, x1v))};
;                 const f32x4 cc = (f32x4){SUM16(DOT4(b2, a3v)), SUM16(DOT4(kp2, a3v)), SUM16(DOT4(b0, r0)), SUM16(DOT4(kp0, r0))};
;                 const f32x4 cd = (f32x4){SUM16(DOT4(Bt, r1)), SUM16(DOT4(Kt, r1)), SUM16(DOT4(b1, r1)), SUM16(DOT4(kp1, r1))};
;                 const float ci = SUM16(DOT4(kp0, a1v));
;                 const f32x4 z0 = r0 * kp0 * prk_, z1 = r1 * kp1 * prk_;
	v_pk_fma_f32 v[10:11], v[92:93], v[10:11], 1.0 op_sel_hi:[1,1,0]
	v_pk_fma_f32 v[12:13], v[90:91], v[12:13], 1.0 op_sel_hi:[1,1,0]
	v_lshlrev_b32_e32 v120, 2, v127
	v_pk_mul_f32 v[106:107], v[18:19], v[106:107] op_sel_hi:[1,0] neg_lo:[0,1] neg_hi:[0,1]
	v_pk_mul_f32 v[78:79], v[78:79], v[116:117]
	v_pk_mul_f32 v[86:87], v[86:87], v[108:109]
	v_pk_mul_f32 v[108:109], v[12:13], v[114:115]
	v_pk_mul_f32 v[112:113], v[10:11], v[112:113]
	v_pk_mul_f32 v[12:13], v[168:169], v[164:165]
	v_pk_mul_f32 v[10:11], v[166:167], v[162:163]
	v_pk_mul_f32 v[116:117], v[172:173], v[98:99]
	v_add3_u32 v121, s1, v130, v120
	v_pk_mul_f32 v[94:95], v[168:169], v[22:23]
	v_pk_mul_f32 v[90:91], v[168:169], v[84:85]
	v_pk_mul_f32 v[114:115], v[170:171], v[106:107]
	v_pk_mul_f32 v[118:119], v[12:13], v[14:15] neg_lo:[0,1] neg_hi:[0,1]
	v_pk_mul_f32 v[168:169], v[12:13], v[116:117]
	v_pk_mul_f32 v[172:173], v[82:83], v[12:13]
	ds_write_b128 v121, v[10:13]
	v_add_u32_e32 v12, s1, v131
	v_pk_mul_f32 v[18:19], v[14:15], v[96:97]
	v_pk_mul_f32 v[96:97], v[166:167], v[20:21]
	v_pk_mul_f32 v[92:93], v[166:167], v[80:81]
	v_pk_mul_f32 v[166:167], v[10:11], v[16:17] neg_lo:[0,1] neg_hi:[0,1]
	v_pk_mul_f32 v[170:171], v[10:11], v[114:115]
	v_pk_mul_f32 v[174:175], v[28:29], v[10:11]
	v_add_u32_e32 v10, v12, v120
	ds_write_b128 v10, v[146:149] offset:38144
	v_add3_u32 v10, s1, v132, v120
	v_pk_mul_f32 v[110:111], v[16:17], v[154:155]
	ds_write_b128 v10, v[150:153] offset:38144
	v_add3_u32 v10, s1, v133, v134
	v_mov_b32_e32 v154, v147
	v_mov_b32_e32 v155, v151
	ds_write_b128 v10, v[154:157] offset:4112
	v_mov_b32_e32 v156, v148
	v_mov_b32_e32 v157, v152
	v_mov_b32_e32 v120, v146
	v_mov_b32_e32 v121, v150
	v_mov_b32_e32 v123, v0
	ds_write_b128 v10, v[156:159] offset:4128
	v_mov_b32_e32 v158, v149
	v_mov_b32_e32 v159, v153
	ds_write_b128 v10, v[120:123] offset:4096
	ds_write_b128 v10, v[158:161] offset:4144
	v_add3_u32 v13, v12, v135, v142
	v_cvt_pk_bf16_f32 v10, v96, v92
	v_cvt_pk_bf16_f32 v11, v88, v86
	ds_write_b64 v13, v[10:11] offset:20480
	v_cvt_pk_bf16_f32 v10, v97, v93
	v_cvt_pk_bf16_f32 v11, v89, v87
	ds_write_b64 v13, v[10:11] offset:20512
	v_cvt_pk_bf16_f32 v10, v94, v90
	v_cvt_pk_bf16_f32 v11, v24, v78
	ds_write_b64 v13, v[10:11] offset:20544
	v_cvt_pk_bf16_f32 v10, v95, v91
	v_cvt_pk_bf16_f32 v11, v25, v79
	ds_write_b64 v13, v[10:11] offset:20576
	v_add_u32_e32 v10, v12, v136
	v_add3_u32 v12, v10, v137, v138
	v_cvt_pk_bf16_f32 v10, v166, v167
	v_cvt_pk_bf16_f32 v11, v118, v119
	ds_write_b64 v12, v[10:11] offset:28672
	v_cvt_pk_bf16_f32 v10, v170, v171
	v_cvt_pk_bf16_f32 v11, v168, v169
	v_pk_mul_f32 v[164:165], v[164:165], v[102:103]
	v_pk_mul_f32 v[162:163], v[162:163], v[100:101]
	ds_write_b64 v12, v[10:11] offset:28800
	v_cvt_pk_bf16_f32 v10, v162, v163
	v_cvt_pk_bf16_f32 v11, v164, v165
	ds_write_b64 v12, v[10:11] offset:28928
	v_cvt_pk_bf16_f32 v10, v174, v175
	v_cvt_pk_bf16_f32 v11, v172, v173
	ds_write_b64 v12, v[10:11] offset:29056
	v_mul_f32_e64 v10, v97, -v17
	v_mul_f32_e64 v11, v95, -v15
	v_fma_f32 v10, v96, -v16, v10
	v_fma_f32 v11, v94, -v14, v11
	v_add_f32_e32 v10, v10, v11
	v_mul_f32_e64 v11, v93, -v17
	v_mul_f32_e64 v12, v91, -v15
	v_fma_f32 v11, v92, -v16, v11
	v_fma_f32 v12, v90, -v14, v12
	v_add_f32_e32 v11, v11, v12
	v_mul_f32_e64 v12, v89, -v17
	v_mul_f32_e64 v13, v25, -v15
	v_fma_f32 v12, v88, -v16, v12
	v_fma_f32 v13, v24, -v14, v13
	v_add_f32_e32 v12, v12, v13
	v_mul_f32_e64 v13, v87, -v17
	v_mul_f32_e64 v15, v79, -v15
	v_fma_f32 v13, v86, -v16, v13
	v_fma_f32 v14, v78, -v14, v15
	v_add_f32_e32 v13, v13, v14
	v_mul_f32_e32 v14, v97, v115
	v_mul_f32_e32 v15, v95, v117
	v_fmac_f32_e32 v14, v96, v114
	v_fmac_f32_e32 v15, v94, v116
	v_add_f32_e32 v14, v14, v15
	v_mul_f32_e32 v15, v93, v115
	v_mul_f32_e32 v16, v91, v117
	v_mul_f32_e32 v21, v21, v101
	v_fmac_f32_e32 v15, v92, v114
	v_fmac_f32_e32 v16, v90, v116
	v_fmac_f32_e32 v21, v20, v100
	v_mul_f32_e32 v20, v23, v103
	v_add_f32_e32 v15, v15, v16
	v_mul_f32_e32 v16, v89, v115
	v_mul_f32_e32 v17, v25, v117
	v_fmac_f32_e32 v20, v22, v102
	v_mul_f32_e32 v89, v89, v29
	v_mul_f32_e32 v25, v25, v83
	v_add_f32_e32 v20, v21, v20
	v_mul_f32_e32 v21, v81, v101
	v_mul_f32_e32 v22, v85, v103
	v_fmac_f32_e32 v89, v88, v28
	v_fmac_f32_e32 v25, v24, v82
	v_fmac_f32_e32 v16, v88, v114
	v_fmac_f32_e32 v17, v24, v116
	v_fmac_f32_e32 v21, v80, v100
	v_fmac_f32_e32 v22, v84, v102
	v_add_f32_e32 v24, v89, v25
	v_mul_f32_e32 v25, v87, v29
	v_mul_f32_e32 v88, v79, v83
	v_add_f32_e32 v21, v21, v22
	v_mul_f32_e32 v22, v97, v29
	v_mul_f32_e32 v23, v95, v83
	v_fmac_f32_e32 v25, v86, v28
	v_fmac_f32_e32 v88, v78, v82
	v_add_f32_e32 v16, v16, v17
	v_mul_f32_e32 v17, v87, v115
	v_fmac_f32_e32 v22, v96, v28
	v_fmac_f32_e32 v23, v94, v82
	v_add_f32_e32 v25, v25, v88
	v_mul_f32_e64 v88, v81, -v105
	v_mul_f32_e64 v27, v85, -v27
	v_fmac_f32_e32 v17, v86, v114
	v_mul_f32_e32 v114, v79, v117
	v_mul_f32_e32 v111, v111, v107
	v_mul_f32_e32 v19, v19, v99
	v_add_f32_e32 v22, v22, v23
	v_mul_f32_e32 v23, v93, v29
	v_fma_f32 v88, v80, -v104, v88
	v_fma_f32 v26, v84, -v26, v27
	v_pk_mul_f32 v[80:81], v[100:101], v[80:81]
	v_pk_mul_f32 v[84:85], v[102:103], v[84:85]
	v_fmac_f32_e32 v114, v78, v116
	v_fmac_f32_e32 v111, v110, v106
	v_fmac_f32_e32 v19, v18, v98
	v_fmac_f32_e32 v23, v92, v28
	v_pk_mul_f32 v[84:85], v[8:9], v[84:85]
	v_pk_mul_f32 v[80:81], v[6:7], v[80:81]
	v_pk_mul_f32 v[28:29], v[28:29], v[86:87]
	v_pk_mul_f32 v[78:79], v[82:83], v[78:79]
	v_add_f32_e32 v18, v111, v19
	v_mul_f32_e32 v19, v113, v107
	v_mul_f32_e32 v99, v109, v99
	v_mul_f32_e32 v91, v91, v83
	v_pk_mul_f32 v[8:9], v[8:9], v[78:79]
	v_pk_mul_f32 v[28:29], v[6:7], v[28:29]
; #define LAS __attribute__((address_space(3)))
; #define SUM16(X) sum16_ns(X)
; __device__ __forceinline__ void scan_unit(Frame& F, const Args& a, int layer, int unit) {
;     ...
;                 const f32x4 ca = (f32x4){SUM16(DOT4(Bt, x0v)), SUM16(DOT4(Kt, x0v)), SUM16(DOT4(b1, x0v)), SUM16(DOT4(kp1, x0v))};
;                 const f32x4 cb = (f32x4){SUM16(DOT4(Bt, x1v)), SUM16(DOT4(Kt, x1v)), SUM16(DOT4(b1, x1v)), SUM16(DOT4(kp1, x1v))};
;                 const f32x4 cc = (f32x4){SUM16(DOT4(b2, a3v)), SUM16(DOT4(kp2, a3v)), SUM16(DOT4(b0, r0)), SUM16(DOT4(kp0, r0))};
;                 const f32x4 cd = (f32x4){SUM16(DOT4(Bt, r1)), SUM16(DOT4(Kt, r1)), SUM16(DOT4(b1, r1)), SUM16(DOT4(kp1, r1))};
;                 const float ci = SUM16(DOT4(kp0, a1v));
;                 const f32x4 z0 = r0 * kp0 * prk_, z1 = r1 * kp1 * prk_;
;                 const float bon0 = SUM16((z0.x + z0.y) + (z0.z + z0.w)), bon1 = SUM16((z1.x + z1.y) + (z1.z + z1.w));
;                 if (c4 == 0) { LAS f32x4* cp = (LAS f32x4*)(buf + SC_C + pr * 20); cp[0] = ca; cp[1] = cb; cp[2] = cc; cp[3] = cd; cp[4] = (f32x4){ci, 0.f, 0.f, 0.f}; }
	v_add_f32_e32 v6, v80, v81
	v_add_f32_e32 v7, v84, v85
	v_fmac_f32_e32 v19, v112, v106
	v_fmac_f32_e32 v99, v108, v98
	v_fmac_f32_e32 v91, v90, v82
	v_add_f32_e32 v6, v6, v7
	v_add_f32_e32 v7, v28, v29
	v_add_f32_e32 v8, v8, v9
	v_add_f32_e32 v17, v17, v114
	v_add_f32_e32 v19, v19, v99
	v_add_f32_e32 v23, v23, v91
	v_add_f32_e32 v26, v88, v26
	v_add_f32_e32 v7, v7, v8
	v_add_f32_dpp v10, v10, v10 quad_perm:[1,0,3,2] row_mask:0xf bank_mask:0xf bound_ctrl:1
	v_add_f32_dpp v11, v11, v11 quad_perm:[1,0,3,2] row_mask:0xf bank_mask:0xf bound_ctrl:1
	v_add_f32_dpp v12, v12, v12 quad_perm:[1,0,3,2] row_mask:0xf bank_mask:0xf bound_ctrl:1
	v_add_f32_dpp v13, v13, v13 quad_perm:[1,0,3,2] row_mask:0xf bank_mask:0xf bound_ctrl:1
	v_add_f32_dpp v14, v14, v14 quad_perm:[1,0,3,2] row_mask:0xf bank_mask:0xf bound_ctrl:1
	v_add_f32_dpp v15, v15, v15 quad_perm:[1,0,3,2] row_mask:0xf bank_mask:0xf bound_ctrl:1
	v_add_f32_dpp v16, v16, v16 quad_perm:[1,0,3,2] row_mask:0xf bank_mask:0xf bound_ctrl:1
	v_add_f32_dpp v17, v17, v17 quad_perm:[1,0,3,2] row_mask:0xf bank_mask:0xf bound_ctrl:1
	v_add_f32_dpp v18, v18, v18 quad_perm:[1,0,3,2] row_mask:0xf bank_mask:0xf bound_ctrl:1
	v_add_f32_dpp v19, v19, v19 quad_perm:[1,0,3,2] row_mask:0xf bank_mask:0xf bound_ctrl:1
	v_add_f32_dpp v20, v20, v20 quad_perm:[1,0,3,2] row_mask:0xf bank_mask:0xf bound_ctrl:1
	v_add_f32_dpp v21, v21, v21 quad_perm:[1,0,3,2] row_mask:0xf bank_mask:0xf bound_ctrl:1
	v_add_f32_dpp v22, v22, v22 quad_perm:[1,0,3,2] row_mask:0xf bank_mask:0xf bound_ctrl:1
	v_add_f32_dpp v23, v23, v23 quad_perm:[1,0,3,2] row_mask:0xf bank_mask:0xf bound_ctrl:1
	v_add_f32_dpp v24, v24, v24 quad_perm:[1,0,3,2] row_mask:0xf bank_mask:0xf bound_ctrl:1
	v_add_f32_dpp v25, v25, v25 quad_perm:[1,0,3,2] row_mask:0xf bank_mask:0xf bound_ctrl:1
	v_add_f32_dpp v26, v26, v26 quad_perm:[1,0,3,2] row_mask:0xf bank_mask:0xf bound_ctrl:1
	v_add_f32_dpp v6, v6, v6 quad_perm:[1,0,3,2] row_mask:0xf bank_mask:0xf bound_ctrl:1
	v_add_f32_dpp v7, v7, v7 quad_perm:[1,0,3,2] row_mask:0xf bank_mask:0xf bound_ctrl:1
	s_nop 1
	v_add_f32_dpp v10, v10, v10 quad_perm:[2,3,0,1] row_mask:0xf bank_mask:0xf bound_ctrl:1
	v_add_f32_dpp v11, v11, v11 quad_perm:[2,3,0,1] row_mask:0xf bank_mask:0xf bound_ctrl:1
	v_add_f32_dpp v12, v12, v12 quad_perm:[2,3,0,1] row_mask:0xf bank_mask:0xf bound_ctrl:1
	v_add_f32_dpp v13, v13, v13 quad_perm:[2,3,0,1] row_mask:0xf bank_mask:0xf bound_ctrl:1
	v_add_f32_dpp v14, v14, v14 quad_perm:[2,3,0,1] row_mask:0xf bank_mask:0xf bound_ctrl:1
	v_add_f32_dpp v15, v15, v15 quad_perm:[2,3,0,1] row_mask:0xf bank_mask:0xf bound_ctrl:1
	v_add_f32_dpp v16, v16, v16 quad_perm:[2,3,0,1] row_mask:0xf bank_mask:0xf bound_ctrl:1
	v_add_f32_dpp v17, v17, v17 quad_perm:[2,3,0,1] row_mask:0xf bank_mask:0xf bound_ctrl:1
	v_add_f32_dpp v18, v18, v18 quad_perm:[2,3,0,1] row_mask:0xf bank_mask:0xf bound_ctrl:1
	v_add_f32_dpp v19, v19, v19 quad_perm:[2,3,0,1] row_mask:0xf bank_mask:0xf bound_ctrl:1
	v_add_f32_dpp v20, v20, v20 quad_perm:[2,3,0,1] row_mask:0xf bank_mask:0xf bound_ctrl:1
	v_add_f32_dpp v21, v21, v21 quad_perm:[2,3,0,1] row_mask:0xf bank_mask:0xf bound_ctrl:1
	v_add_f32_dpp v22, v22, v22 quad_perm:[2,3,0,1] row_mask:0xf bank_mask:0xf bound_ctrl:1
	v_add_f32_dpp v23, v23, v23 quad_perm:[2,3,0,1] row_mask:0xf bank_mask:0xf bound_ctrl:1
	v_add_f32_dpp v24, v24, v24 quad_perm:[2,3,0,1] row_mask:0xf bank_mask:0xf bound_ctrl:1
	v_add_f32_dpp v25, v25, v25 quad_perm:[2,3,0,1] row_mask:0xf bank_mask:0xf bound_ctrl:1
	v_add_f32_dpp v26, v26, v26 quad_perm:[2,3,0,1] row_mask:0xf bank_mask:0xf bound_ctrl:1
	v_add_f32_dpp v6, v6, v6 quad_perm:[2,3,0,1] row_mask:0xf bank_mask:0xf bound_ctrl:1
	v_add_f32_dpp v7, v7, v7 quad_perm:[2,3,0,1] row_mask:0xf bank_mask:0xf bound_ctrl:1
	s_nop 1
	v_add_f32_dpp v10, v10, v10 row_half_mirror row_mask:0xf bank_mask:0xf bound_ctrl:1
	v_add_f32_dpp v11, v11, v11 row_half_mirror row_mask:0xf bank_mask:0xf bound_ctrl:1
	v_add_f32_dpp v12, v12, v12 row_half_mirror row_mask:0xf bank_mask:0xf bound_ctrl:1
	v_add_f32_dpp v13, v13, v13 row_half_mirror row_mask:0xf bank_mask:0xf bound_ctrl:1
	v_add_f32_dpp v14, v14, v14 row_half_mirror row_mask:0xf bank_mask:0xf bound_ctrl:1
	v_add_f32_dpp v15, v15, v15 row_half_mirror row_mask:0xf bank_mask:0xf bound_ctrl:1
	v_add_f32_dpp v16, v16, v16 row_half_mirror row_mask:0xf bank_mask:0xf bound_ctrl:1
	v_add_f32_dpp v17, v17, v17 row_half_mirror row_mask:0xf bank_mask:0xf bound_ctrl:1
	v_add_f32_dpp v18, v18, v18 row_half_mirror row_mask:0xf bank_mask:0xf bound_ctrl:1
	v_add_f32_dpp v19, v19, v19 row_half_mirror row_mask:0xf bank_mask:0xf bound_ctrl:1
	v_add_f32_dpp v20, v20, v20 row_half_mirror row_mask:0xf bank_mask:0xf bound_ctrl:1
	v_add_f32_dpp v21, v21, v21 row_half_mirror row_mask:0xf bank_mask:0xf bound_ctrl:1
	v_add_f32_dpp v22, v22, v22 row_half_mirror row_mask:0xf bank_mask:0xf bound_ctrl:1
	v_add_f32_dpp v23, v23, v23 row_half_mirror row_mask:0xf bank_mask:0xf bound_ctrl:1
	v_add_f32_dpp v24, v24, v24 row_half_mirror row_mask:0xf bank_mask:0xf bound_ctrl:1
	v_add_f32_dpp v25, v25, v25 row_half_mirror row_mask:0xf bank_mask:0xf bound_ctrl:1
	v_add_f32_dpp v26, v26, v26 row_half_mirror row_mask:0xf bank_mask:0xf bound_ctrl:1
	v_add_f32_dpp v6, v6, v6 row_half_mirror row_mask:0xf bank_mask:0xf bound_ctrl:1
	v_add_f32_dpp v7, v7, v7 row_half_mirror row_mask:0xf bank_mask:0xf bound_ctrl:1
	s_nop 1
	v_add_f32_dpp v10, v10, v10 row_mirror row_mask:0xf bank_mask:0xf bound_ctrl:1
	v_add_f32_dpp v11, v11, v11 row_mirror row_mask:0xf bank_mask:0xf bound_ctrl:1
	v_add_f32_dpp v12, v12, v12 row_mirror row_mask:0xf bank_mask:0xf bound_ctrl:1
	v_add_f32_dpp v13, v13, v13 row_mirror row_mask:0xf bank_mask:0xf bound_ctrl:1
	v_add_f32_dpp v14, v14, v14 row_mirror row_mask:0xf bank_mask:0xf bound_ctrl:1
	v_add_f32_dpp v15, v15, v15 row_mirror row_mask:0xf bank_mask:0xf bound_ctrl:1
	v_add_f32_dpp v16, v16, v16 row_mirror row_mask:0xf bank_mask:0xf bound_ctrl:1
	v_add_f32_dpp v17, v17, v17 row_mirror row_mask:0xf bank_mask:0xf bound_ctrl:1
	v_add_f32_dpp v18, v18, v18 row_mirror row_mask:0xf bank_mask:0xf bound_ctrl:1
	v_add_f32_dpp v19, v19, v19 row_mirror row_mask:0xf bank_mask:0xf bound_ctrl:1
	v_add_f32_dpp v20, v20, v20 row_mirror row_mask:0xf bank_mask:0xf bound_ctrl:1
	v_add_f32_dpp v21, v21, v21 row_mirror row_mask:0xf bank_mask:0xf bound_ctrl:1
	v_add_f32_dpp v22, v22, v22 row_mirror row_mask:0xf bank_mask:0xf bound_ctrl:1
	v_add_f32_dpp v23, v23, v23 row_mirror row_mask:0xf bank_mask:0xf bound_ctrl:1
	v_add_f32_dpp v24, v24, v24 row_mirror row_mask:0xf bank_mask:0xf bound_ctrl:1
	v_add_f32_dpp v25, v25, v25 row_mirror row_mask:0xf bank_mask:0xf bound_ctrl:1
	v_add_f32_dpp v26, v26, v26 row_mirror row_mask:0xf bank_mask:0xf bound_ctrl:1
	v_add_f32_dpp v6, v6, v6 row_mirror row_mask:0xf bank_mask:0xf bound_ctrl:1
	v_add_f32_dpp v7, v7, v7 row_mirror row_mask:0xf bank_mask:0xf bound_ctrl:1
	s_and_saveexec_b64 s[2:3], s[40:41]
	s_cbranch_execz .LBB0_1320
; #define LAS __attribute__((address_space(3)))
; __device__ __forceinline__ void scan_unit(Frame& F, const Args& a, int layer, int unit) {
;     ...
;                 if (c4 == 0) { LAS f32x4* cp = (LAS f32x4*)(buf + SC_C + pr * 20); cp[0] = ca; cp[1] = cb; cp[2] = cc; cp[3] = cd; cp[4] = (f32x4){ci, 0.f, 0.f, 0.f}; }
	v_add_u32_e32 v8, s1, v139
	v_mov_b32_e32 v27, v0
	v_mov_b32_e32 v28, v0
	v_mov_b32_e32 v29, v0
	ds_write_b128 v8, v[10:13] offset:36864
	ds_write_b128 v8, v[14:17] offset:36880
	ds_write_b128 v8, v[18:21] offset:36896
	ds_write_b128 v8, v[22:25] offset:36912
	ds_write_b128 v8, v[26:29] offset:36928
	s_branch .LBB0_1320
